# P9 gathered GEMM: next-unit row-list loads deferred behind counted vmcnt (no full drain in last K iteration), first-unit list loads batched
# speedup vs baseline: 1.0148x; 1.0003x over previous
; #define PG8_STAGE_B(bufoff, gbase) do { if (FP8) { glds16s((gbase), vB[0], ldsb + (unsigned)(bufoff)); glds16s((gbase) + dB1, vB[0], ldsb + (unsigned)(bufoff) + 8192u); } \
;         else PG8_STAGE2(bufoff, gbase, vB[0], vB[1]); } while (0)
; #define PG8_STAGE_A(bufoff, gbase, hh, nx) do { if (FP8 && !GATHER) { glds16s((gbase) + (size_t)(hh) * dA2, vA[0][0], ldsb + (unsigned)(bufoff)); glds16s((gbase) + (size_t)(hh) * dA2 + dA1, vA[0][0], ldsb + (unsigned)(bufoff) + 8192u); } \
;         else PG8_STAGE2(bufoff, gbase, vA[hh][0], vA[hh][1]); } while (0)
; template <bool GATHER, class Epi, class Sched, bool FP8 = false>
; DEV void gemm_phase(LAS char* lds, const Gemm g, const Sched& S, const Epi& E) {
;     ...
;     PG8_GOFF(cur, vA, 0); PG8_GOFF(cur, vA, 1);
;     const char* cA = (const char*)g.A + (GATHER ? (size_t)0 : (size_t)cur.arow * g.lda); const char* cB = (const char*)g.Bt + (size_t)cur.brow * g.ldb;
;     PG8_STAGE_B(PG8_SB(0, 0), cB); PG8_STAGE_B(PG8_SB(0, 1), cB + hstepB); PG8_STAGE_A(PG8_SA(0, 0), cA, 0, false); PG8_STAGE_A(PG8_SA(0, 1), cA, 1, false);
.LBB0_1307:
	s_and_b64 vcc, exec, s[4:5]
	s_cbranch_vccz .LBB0_1337
	s_cmp_ge_i32 s28, s12
	s_cbranch_scc1 .LBB0_1337
	v_bfe_i32 v5, v3, 27, 1
	v_lshlrev_b32_e32 v2, 4, v3
	v_lshrrev_b32_e32 v5, 22, v5
	v_add_u32_e32 v5, v2, v5
	s_add_u32 s4, s8, 0x21710100
	v_and_b32_e32 v5, 0xfffffc00, v5
	s_addc_u32 s5, s9, 0
	v_sub_u32_e32 v2, v2, v5
	s_add_u32 s16, s8, 0x1510100
	v_ashrrev_i32_e32 v4, 31, v3
	v_lshrrev_b32_e32 v5, 4, v2
	s_addc_u32 s17, s9, 0
	v_lshrrev_b32_e32 v4, 26, v4
	v_bitop3_b32 v5, v5, v2, 32 bitop3:0x6c
	v_ashrrev_i32_e32 v2, 31, v2
	s_add_u32 s6, s8, 0x2ad60100
	v_add_u32_e32 v4, v3, v4
	v_lshrrev_b32_e32 v2, 26, v2
	s_addc_u32 s7, s9, 0
	v_ashrrev_i32_e32 v4, 6, v4
	v_add_u32_e32 v2, v5, v2
	s_ashr_i32 s21, s19, 6
	v_lshlrev_b32_e32 v6, 3, v4
	v_ashrrev_i32_e32 v2, 6, v2
	s_lshl_b32 s2, s21, 10
	v_writelane_b32 v254, s18, 61
	v_and_b32_e32 v6, -16, v6
	v_mul_i32_i24_e32 v7, 64, v2
	s_add_i32 s18, s2, 0
	s_mov_b32 s2, s72
	v_add_u32_e32 v6, v2, v6
	v_sub_u32_e32 v5, v5, v7
	v_writelane_b32 v254, s2, 63
	v_lshlrev_b32_e32 v4, 5, v4
	v_ashrrev_i16_sdwa v5, v218, sext(v5) dst_sel:DWORD dst_unused:UNUSED_PAD src0_sel:DWORD src1_sel:BYTE_0
	v_lshlrev_b32_e32 v7, 1, v6
	v_lshrrev_b32_e32 v6, 2, v6
	v_writelane_b32 v255, s3, 0
	s_and_b32 s2, s28, -4
	v_and_b32_e32 v4, 32, v4
	v_bfe_i32 v5, v5, 0, 16
	v_and_b32_e32 v6, 4, v6
	v_and_b32_e32 v2, 3, v2
	v_and_b32_e32 v7, 0x3fffd8, v7
	s_add_i32 s2, s2, 0
	v_or3_b32 v2, v2, v6, v7
	v_add_lshl_u32 v4, v4, v5, 1
	s_add_i32 s2, s2, 0x23000
	v_lshl_add_u32 v204, v2, 10, v4
	v_mov_b32_e32 v2, s2
	ds_read_b32 v2, v2
	s_lshl_b32 s3, s72, 16
	s_and_b32 s96, s28, 3
	s_ashr_i32 s97, s28, 2
	v_writelane_b32 v254, s3, 49
	s_waitcnt lgkmcnt(0)
	v_lshlrev_b32_e32 v4, 2, v2
	v_add_u32_e32 v4, 0, v4
	v_add_u32_e32 v5, 0x23c00, v4
	ds_read_b32 v5, v5
	v_readfirstlane_b32 s2, v2
	s_lshl_b32 s2, s2, 10
	s_add_i32 s2, s2, s3
	s_lshl_b32 s3, s96, 8
	s_waitcnt lgkmcnt(0)
	v_sub_u32_e32 v5, s97, v5
	s_or_b32 s28, s2, s3
	s_mov_b32 s2, 0x8200
	v_mul_lo_u32 v2, v2, s2
	v_lshlrev_b32_e32 v5, 8, v5
	v_add_u32_e32 v6, v5, v2
	v_add_u32_e32 v2, 0x23d40, v4
	ds_read_b32 v2, v2
	s_ashr_i32 s29, s28, 31
	s_lshl_b64 s[38:39], s[28:29], 10
	s_ashr_i32 s20, s19, 8
	s_add_u32 s52, s16, s38
	s_waitcnt lgkmcnt(0)
	v_sub_u32_e32 v7, v2, v5
	v_mov_b32_e32 v2, v246
	s_addc_u32 s53, s17, s39
	v_ashrrev_i32_e32 v5, 31, v2
	v_lshrrev_b32_e32 v5, 26, v5
	v_lshlrev_b32_e32 v4, 4, v2
	v_add_u32_e32 v5, v2, v5
	v_bfe_i32 v2, v2, 27, 1
	v_lshrrev_b32_e32 v2, 22, v2
	v_add_u32_e32 v2, v4, v2
	v_and_b32_e32 v2, 0xfffffc00, v2
	v_sub_u32_e32 v2, v4, v2
	v_lshrrev_b32_e32 v4, 4, v2
	v_bitop3_b32 v4, v4, v2, 32 bitop3:0x6c
	v_ashrrev_i32_e32 v2, 31, v2
	v_ashrrev_i32_e32 v5, 6, v5
	v_lshrrev_b32_e32 v2, 26, v2
	v_lshlrev_b32_e32 v8, 3, v5
	v_add_u32_e32 v2, v4, v2
	v_and_b32_e32 v8, -16, v8
	v_ashrrev_i32_e32 v2, 6, v2
	v_add_u32_e32 v8, v2, v8
	v_mul_i32_i24_e32 v2, 64, v2
	v_sub_u32_e32 v2, v4, v2
	v_cmp_lt_i32_e32 vcc, v8, v7
	v_lshlrev_b32_e32 v5, 5, v5
	v_ashrrev_i16_sdwa v2, v218, sext(v2) dst_sel:DWORD dst_unused:UNUSED_PAD src0_sel:DWORD src1_sel:BYTE_0
	v_cndmask_b32_e32 v4, 0, v8, vcc
	v_and_b32_e32 v5, 32, v5
	v_bfe_i32 v2, v2, 0, 16
	v_add_u32_e32 v4, v4, v6
	v_add_lshl_u32 v2, v5, v2, 1
	v_ashrrev_i32_e32 v5, 31, v4
	v_lshl_add_u64 v[4:5], v[4:5], 2, s[6:7]
	global_load_dword v224, v[4:5], off
	v_add_u32_e32 v4, 64, v8
	v_cmp_lt_i32_e32 vcc, v4, v7
	s_nop 1
	v_cndmask_b32_e32 v4, 0, v4, vcc
	v_add_u32_e32 v4, v4, v6
	v_ashrrev_i32_e32 v5, 31, v4
	v_lshl_add_u64 v[4:5], v[4:5], 2, s[6:7]
	global_load_dword v225, v[4:5], off
	v_mov_b32_e32 v2, v246
	s_nop 0
	v_ashrrev_i32_e32 v5, 31, v2
	v_lshrrev_b32_e32 v5, 26, v5
	v_lshlrev_b32_e32 v4, 4, v2
	v_add_u32_e32 v5, v2, v5
	v_bfe_i32 v2, v2, 27, 1
	v_lshrrev_b32_e32 v2, 22, v2
	v_add_u32_e32 v2, v4, v2
	v_and_b32_e32 v2, 0xfffffc00, v2
	v_sub_u32_e32 v2, v4, v2
	v_lshrrev_b32_e32 v4, 4, v2
	v_bitop3_b32 v4, v4, v2, 32 bitop3:0x6c
	v_ashrrev_i32_e32 v2, 31, v2
	v_lshrrev_b32_e32 v2, 26, v2
	v_ashrrev_i32_e32 v5, 6, v5
	v_add_u32_e32 v2, v4, v2
	v_lshlrev_b32_e32 v8, 3, v5
	v_ashrrev_i32_e32 v2, 6, v2
	v_and_b32_e32 v8, -16, v8
	v_mul_i32_i24_e32 v9, 64, v2
	v_sub_u32_e32 v4, v4, v9
	v_add_u32_e32 v8, v8, v2
	v_lshlrev_b32_e32 v5, 5, v5
	v_ashrrev_i16_sdwa v4, v218, sext(v4) dst_sel:DWORD dst_unused:UNUSED_PAD src0_sel:DWORD src1_sel:BYTE_0
	v_add_u32_e32 v9, 0x80, v8
	v_and_b32_e32 v5, 32, v5
	v_bfe_i32 v4, v4, 0, 16
	v_cmp_lt_i32_e32 vcc, v9, v7
	v_add_lshl_u32 v2, v5, v4, 1
	s_nop 0
	v_cndmask_b32_e32 v4, 0, v9, vcc
	v_add_u32_e32 v4, v4, v6
	v_ashrrev_i32_e32 v5, 31, v4
	v_lshl_add_u64 v[4:5], v[4:5], 2, s[6:7]
	global_load_dword v227, v[4:5], off
	v_add_u32_e32 v4, 0xc0, v8
	v_cmp_lt_i32_e32 vcc, v4, v7
	s_nop 1
	v_cndmask_b32_e32 v4, 0, v4, vcc
	v_add_u32_e32 v4, v4, v6
	v_ashrrev_i32_e32 v5, 31, v4
	v_lshl_add_u64 v[4:5], v[4:5], 2, s[6:7]
	global_load_dword v228, v[4:5], off
	s_waitcnt vmcnt(0)
	v_mul_lo_u32 v196, v224, s95
	v_mul_lo_u32 v198, v225, s95
	v_mul_lo_u32 v200, v227, s95
	v_mul_lo_u32 v202, v228, s95
	v_add_u32_e32 v196, v196, v2
	v_add_u32_e32 v198, v198, v2
	v_add_u32_e32 v200, v200, v2
	v_add_u32_e32 v202, v202, v2
	s_add_i32 s28, s18, 0x10000
	s_add_u32 s36, s52, 0x20000
	s_mov_b32 s2, m0
	s_mov_b32 m0, s28
	s_nop 0
	global_load_lds_dwordx4 v204, s[52:53]
	s_mov_b32 m0, s2
	s_addc_u32 s37, s53, 0
	s_add_i32 s30, s18, 0x12000
	s_mov_b32 s2, m0
	s_mov_b32 m0, s30
	s_nop 0
	global_load_lds_dwordx4 v204, s[36:37]
	s_mov_b32 m0, s2
	s_add_u32 s36, s52, 0x8000
	s_addc_u32 s37, s53, 0
	s_add_i32 s33, s18, 0x14000
	s_mov_b32 s2, m0
	s_mov_b32 m0, s33
	s_nop 0
	global_load_lds_dwordx4 v204, s[36:37]
	s_mov_b32 m0, s2
	s_add_u32 s38, s52, 0x28000
	s_addc_u32 s39, s53, 0
	s_add_i32 s36, s18, 0x16000
	s_mov_b32 s2, m0
	s_mov_b32 m0, s36
	s_nop 0
	global_load_lds_dwordx4 v204, s[38:39]
	s_mov_b32 m0, s2
	s_add_i32 s37, s18, 0x2000
	s_mov_b32 s2, m0
	s_mov_b32 m0, s18
	s_nop 0
	global_load_lds_dwordx4 v196, s[4:5]
	s_mov_b32 m0, s2
	s_add_i32 s62, s18, 0x4000
	s_mov_b32 s2, m0
	s_mov_b32 m0, s37
	s_nop 0
	global_load_lds_dwordx4 v198, s[4:5]
	s_mov_b32 m0, s2
	s_add_i32 s63, s18, 0x6000
	s_mov_b32 s2, m0
	s_mov_b32 m0, s62
	s_nop 0
	global_load_lds_dwordx4 v200, s[4:5]
	s_mov_b32 m0, s2
	s_cmp_eq_u32 s20, 1
	s_mov_b32 s2, m0
	s_mov_b32 m0, s63
	s_nop 0
	global_load_lds_dwordx4 v202, s[4:5]
	s_mov_b32 m0, s2
	s_cselect_b64 s[2:3], -1, 0
	v_writelane_b32 v254, s2, 59
	s_cmp_lg_u32 s20, 1
	s_nop 0
	v_writelane_b32 v254, s3, 60
	s_cbranch_scc1 .LBB0_1311
	s_barrier

; #define PG8_STAGE_B(bufoff, gbase) do { if (FP8) { glds16s((gbase), vB[0], ldsb + (unsigned)(bufoff)); glds16s((gbase) + dB1, vB[0], ldsb + (unsigned)(bufoff) + 8192u); } \
;         else PG8_STAGE2(bufoff, gbase, vB[0], vB[1]); } while (0)
; #define PG8_STAGE_A(bufoff, gbase, hh, nx) do { if (FP8 && !GATHER) { glds16s((gbase) + (size_t)(hh) * dA2, vA[0][0], ldsb + (unsigned)(bufoff)); glds16s((gbase) + (size_t)(hh) * dA2 + dA1, vA[0][0], ldsb + (unsigned)(bufoff) + 8192u); } \
;         else PG8_STAGE2(bufoff, gbase, vA[hh][0], vA[hh][1]); } while (0)
; #define PG8_LDA(dst, b, h) do { if (FP8) { _Pragma("unroll") for (int m = 0; m < 4; ++m) dst##8[m] = PG8_LD8(lds + PG8_SA(b, h) + aoff + m * 2048); } else { \
;         _Pragma("unroll") for (int m = 0; m < 4; ++m) _Pragma("unroll") for (int k = 0; k < 2; ++k) dst[m][k] = *(const LAS bf16x8*)(lds + PG8_SA(b, h) + aoff + m * 2048 + k * 1024); } } while (0)
; #define PG8_WAIT_V(n) asm volatile("s_waitcnt vmcnt(" #n ")" ::: "memory")
; template <bool GATHER, class Epi, class Sched, bool FP8 = false>
; DEV void gemm_phase(LAS char* lds, const Gemm g, const Sched& S, const Epi& E) {
;     ...
;         for (int t = 0; t < nt; t += 2) {
;             const bool last = (t == nt - 2), lastn = last && has_next;
;             const char* a1 = cA + (size_t)(t + 1) * kstep;
;             const char* a2 = last ? nA : cA + (size_t)(t + 2) * kstep; const char* b2 = last ? nB : cB + (size_t)(t + 2) * kstep;
;             const char* a3 = a2 + kstep; const char* b3 = b2 + kstep;
;             if (GATHER && lastn) PG8_GOFF(nxt, vA, 0);
;             PG8_LDB(B0, 0, 0); PG8_LDB(B1, 0, 1); PG8_SCHED; PG8_LDA(At, 0, 0); PG8_STAGE_A(PG8_SA(1, 1), a1, 1, false);
;             if (GATHER && lastn) PG8_GOFF(nxt, vA, 1);
;             PG8_WAIT_V(8); PG8_WAIT_L(0); PG8_BAR; PG8_MM(0, 0, At, B0); PG8_MM(0, 1, At, B1); PG8_BAR; PG8_SCHED;
;             PG8_LDA(At, 0, 1); PG8_STAGE_B(PG8_SB(0, 0), b2); PG8_STAGE_B(PG8_SB(0, 1), b2 + hstepB); PG8_STAGE_A(PG8_SA(0, 0), a2, 0, lastn);
;             PG8_WAIT_V(8); PG8_WAIT_L(0); PG8_BAR; PG8_MM(1, 0, At, B0); PG8_MM(1, 1, At, B1); PG8_BAR; PG8_SCHED;
;             PG8_LDB(B0, 1, 0); PG8_LDB(B1, 1, 1); PG8_SCHED; PG8_LDA(At, 1, 0); PG8_STAGE_A(PG8_SA(0, 1), a2, 1, lastn);
;             PG8_WAIT_V(8); PG8_WAIT_L(0); PG8_BAR; PG8_MM(0, 0, At, B0); PG8_MM(0, 1, At, B1); PG8_BAR; PG8_SCHED;
.LBB0_1325:
	s_add_i32 s19, s19, 2
	s_and_b64 s[20:21], s[58:59], exec
	s_cselect_b32 s3, 0, s56
	s_cselect_b32 s2, 0, s57
	s_add_u32 s60, s4, s3
	s_addc_u32 s61, s5, s2
	s_add_u32 s2, s52, s56
	s_addc_u32 s3, s53, s57
	s_and_b64 s[20:21], s[58:59], exec
	s_waitcnt vmcnt(8)
	s_cselect_b32 s21, s49, s3
	s_cselect_b32 s20, s29, s2
	s_add_u32 s42, s60, 0x80
	s_waitcnt lgkmcnt(0)
	s_addc_u32 s43, s61, 0
	s_add_u32 s58, s20, 0x80
	s_addc_u32 s59, s21, 0
	s_barrier
	s_setprio 1
	s_waitcnt lgkmcnt(6)
	v_mfma_scale_f32_16x16x128_f8f6f4 v[192:195], v[18:25], v[58:65], v[192:195], v1, v209 op_sel_hi:[0,0,0]
	v_mfma_scale_f32_16x16x128_f8f6f4 v[184:187], v[26:33], v[58:65], v[184:187], v1, v209 op_sel_hi:[0,0,0]
	s_waitcnt lgkmcnt(4)
	v_mfma_scale_f32_16x16x128_f8f6f4 v[174:177], v[18:25], v[50:57], v[174:177], v1, v209 op_sel_hi:[0,0,0]
	v_mfma_scale_f32_16x16x128_f8f6f4 v[166:169], v[26:33], v[50:57], v[166:169], v1, v209 op_sel_hi:[0,0,0]
	s_waitcnt lgkmcnt(2)
	v_mfma_scale_f32_16x16x128_f8f6f4 v[158:161], v[18:25], v[42:49], v[158:161], v1, v209 op_sel_hi:[0,0,0]
	v_mfma_scale_f32_16x16x128_f8f6f4 v[150:153], v[26:33], v[42:49], v[150:153], v1, v209 op_sel_hi:[0,0,0]
	s_waitcnt lgkmcnt(0)
	v_mfma_scale_f32_16x16x128_f8f6f4 v[142:145], v[18:25], v[34:41], v[142:145], v1, v209 op_sel_hi:[0,0,0]
	v_mfma_scale_f32_16x16x128_f8f6f4 v[134:137], v[26:33], v[34:41], v[134:137], v1, v209 op_sel_hi:[0,0,0]
	s_setprio 0
	s_setprio 1
	v_mfma_scale_f32_16x16x128_f8f6f4 v[188:191], v[2:9], v[58:65], v[188:191], v1, v209 op_sel_hi:[0,0,0]
	v_mfma_scale_f32_16x16x128_f8f6f4 v[180:183], v[10:17], v[58:65], v[180:183], v1, v209 op_sel_hi:[0,0,0]
	v_mfma_scale_f32_16x16x128_f8f6f4 v[170:173], v[2:9], v[50:57], v[170:173], v1, v209 op_sel_hi:[0,0,0]
	v_mfma_scale_f32_16x16x128_f8f6f4 v[162:165], v[10:17], v[50:57], v[162:165], v1, v209 op_sel_hi:[0,0,0]
	v_mfma_scale_f32_16x16x128_f8f6f4 v[154:157], v[2:9], v[42:49], v[154:157], v1, v209 op_sel_hi:[0,0,0]
	v_mfma_scale_f32_16x16x128_f8f6f4 v[146:149], v[10:17], v[42:49], v[146:149], v1, v209 op_sel_hi:[0,0,0]
	v_mfma_scale_f32_16x16x128_f8f6f4 v[138:141], v[2:9], v[34:41], v[138:141], v1, v209 op_sel_hi:[0,0,0]
	v_mfma_scale_f32_16x16x128_f8f6f4 v[130:133], v[10:17], v[34:41], v[130:133], v1, v209 op_sel_hi:[0,0,0]
	s_setprio 0
	s_barrier
	s_add_u32 s38, s20, 0x20000
	ds_read_b128 v[34:37], v219 offset:16384
	ds_read_b128 v[38:41], v219 offset:17408
	ds_read_b128 v[42:45], v219 offset:18432
	ds_read_b128 v[46:49], v219 offset:19456
	ds_read_b128 v[50:53], v219 offset:20480
	ds_read_b128 v[54:57], v219 offset:21504
	ds_read_b128 v[58:61], v219 offset:22528
	ds_read_b128 v[62:65], v219 offset:23552
	s_mov_b32 s2, m0
	s_mov_b32 m0, s28
	s_nop 0
	global_load_lds_dwordx4 v204, s[20:21]
	s_mov_b32 m0, s2
	s_addc_u32 s39, s21, 0
	s_mov_b32 s2, m0
	s_mov_b32 m0, s30
	s_nop 0
	global_load_lds_dwordx4 v204, s[38:39]
	s_mov_b32 m0, s2
	s_add_u32 s38, s20, 0x8000
	s_addc_u32 s39, s21, 0
	s_mov_b32 s2, m0
	s_mov_b32 m0, s33
	s_nop 0
	global_load_lds_dwordx4 v204, s[38:39]
	s_mov_b32 m0, s2
	s_add_u32 s38, s20, 0x28000
	s_addc_u32 s39, s21, 0
	s_mov_b32 s2, m0
	s_mov_b32 m0, s36
	s_nop 0
	global_load_lds_dwordx4 v204, s[38:39]
	s_mov_b32 m0, s2
	s_nop 0
	s_cmp_eq_u32 s100, 0
	s_cbranch_scc1 .Lp9_g0_skip
	s_waitcnt vmcnt(8)
	v_mul_lo_u32 v196, v224, s95
	v_mul_lo_u32 v198, v225, s95
	v_add_u32_e32 v196, v196, v226
	v_add_u32_e32 v198, v198, v226
.Lp9_g0_skip:
	s_mov_b32 s2, m0
	s_mov_b32 m0, s18
	s_nop 0
	global_load_lds_dwordx4 v196, s[60:61]
	s_mov_b32 m0, s2
	s_nop 0
	s_mov_b32 s2, m0
	s_mov_b32 m0, s37
	s_nop 0
	global_load_lds_dwordx4 v198, s[60:61]
	s_mov_b32 m0, s2
	s_waitcnt vmcnt(8)
	s_waitcnt lgkmcnt(0)
	s_barrier
	s_setprio 1
	s_waitcnt lgkmcnt(6)
	v_mfma_scale_f32_16x16x128_f8f6f4 v[126:129], v[18:25], v[34:41], v[126:129], v1, v209 op_sel_hi:[0,0,0]
	v_mfma_scale_f32_16x16x128_f8f6f4 v[118:121], v[26:33], v[34:41], v[118:121], v1, v209 op_sel_hi:[0,0,0]
	s_waitcnt lgkmcnt(4)
	v_mfma_scale_f32_16x16x128_f8f6f4 v[110:113], v[18:25], v[42:49], v[110:113], v1, v209 op_sel_hi:[0,0,0]
	v_mfma_scale_f32_16x16x128_f8f6f4 v[102:105], v[26:33], v[42:49], v[102:105], v1, v209 op_sel_hi:[0,0,0]
	s_waitcnt lgkmcnt(2)
	v_mfma_scale_f32_16x16x128_f8f6f4 v[94:97], v[18:25], v[50:57], v[94:97], v1, v209 op_sel_hi:[0,0,0]
	v_mfma_scale_f32_16x16x128_f8f6f4 v[86:89], v[26:33], v[50:57], v[86:89], v1, v209 op_sel_hi:[0,0,0]
	s_waitcnt lgkmcnt(0)
	v_mfma_scale_f32_16x16x128_f8f6f4 v[78:81], v[18:25], v[58:65], v[78:81], v1, v209 op_sel_hi:[0,0,0]
	v_mfma_scale_f32_16x16x128_f8f6f4 v[70:73], v[26:33], v[58:65], v[70:73], v1, v209 op_sel_hi:[0,0,0]
	s_setprio 0
	s_setprio 1
	v_mfma_scale_f32_16x16x128_f8f6f4 v[122:125], v[2:9], v[34:41], v[122:125], v1, v209 op_sel_hi:[0,0,0]
	v_mfma_scale_f32_16x16x128_f8f6f4 v[114:117], v[10:17], v[34:41], v[114:117], v1, v209 op_sel_hi:[0,0,0]
	v_mfma_scale_f32_16x16x128_f8f6f4 v[106:109], v[2:9], v[42:49], v[106:109], v1, v209 op_sel_hi:[0,0,0]
	v_mfma_scale_f32_16x16x128_f8f6f4 v[98:101], v[10:17], v[42:49], v[98:101], v1, v209 op_sel_hi:[0,0,0]
	v_mfma_scale_f32_16x16x128_f8f6f4 v[90:93], v[2:9], v[50:57], v[90:93], v1, v209 op_sel_hi:[0,0,0]
	v_mfma_scale_f32_16x16x128_f8f6f4 v[82:85], v[10:17], v[50:57], v[82:85], v1, v209 op_sel_hi:[0,0,0]
	v_mfma_scale_f32_16x16x128_f8f6f4 v[74:77], v[2:9], v[58:65], v[74:77], v1, v209 op_sel_hi:[0,0,0]
	v_mfma_scale_f32_16x16x128_f8f6f4 v[66:69], v[10:17], v[58:65], v[66:69], v1, v209 op_sel_hi:[0,0,0]
	s_setprio 0
	s_barrier
	v_add_u32_e32 v14, 0x18000, v205
	v_add_u32_e32 v30, 0x1c000, v205
	ds_read_b128 v[2:5], v14
	ds_read_b128 v[6:9], v14 offset:1024
	ds_read_b128 v[10:13], v14 offset:2048
	ds_read_b128 v[14:17], v14 offset:3072
	ds_read_b128 v[18:21], v30
	ds_read_b128 v[22:25], v30 offset:1024
	ds_read_b128 v[26:29], v30 offset:2048
	ds_read_b128 v[30:33], v30 offset:3072
	ds_read_b128 v[34:37], v219 offset:32768
	ds_read_b128 v[38:41], v219 offset:33792
	ds_read_b128 v[42:45], v219 offset:34816
	ds_read_b128 v[46:49], v219 offset:35840
	ds_read_b128 v[50:53], v219 offset:36864
	ds_read_b128 v[54:57], v219 offset:37888
	ds_read_b128 v[58:61], v219 offset:38912
	ds_read_b128 v[62:65], v219 offset:39936
	s_cmp_eq_u32 s100, 0
	s_cbranch_scc1 .Lp9_g1_skip
	s_waitcnt vmcnt(6)
	v_mul_lo_u32 v200, v227, s95
	v_mul_lo_u32 v202, v228, s95
	v_add_u32_e32 v200, v200, v226
	v_add_u32_e32 v202, v202, v226
; #define PG8_STAGE_B(bufoff, gbase) do { if (FP8) { glds16s((gbase), vB[0], ldsb + (unsigned)(bufoff)); glds16s((gbase) + dB1, vB[0], ldsb + (unsigned)(bufoff) + 8192u); } \
;         else PG8_STAGE2(bufoff, gbase, vB[0], vB[1]); } while (0)
; #define PG8_STAGE_A(bufoff, gbase, hh, nx) do { if (FP8 && !GATHER) { glds16s((gbase) + (size_t)(hh) * dA2, vA[0][0], ldsb + (unsigned)(bufoff)); glds16s((gbase) + (size_t)(hh) * dA2 + dA1, vA[0][0], ldsb + (unsigned)(bufoff) + 8192u); } \
;         else PG8_STAGE2(bufoff, gbase, vA[hh][0], vA[hh][1]); } while (0)
; #define PG8_LDA(dst, b, h) do { if (FP8) { _Pragma("unroll") for (int m = 0; m < 4; ++m) dst##8[m] = PG8_LD8(lds + PG8_SA(b, h) + aoff + m * 2048); } else { \
;         _Pragma("unroll") for (int m = 0; m < 4; ++m) _Pragma("unroll") for (int k = 0; k < 2; ++k) dst[m][k] = *(const LAS bf16x8*)(lds + PG8_SA(b, h) + aoff + m * 2048 + k * 1024); } } while (0)
; #define PG8_LDB(dst, b, h) do { if (FP8) { _Pragma("unroll") for (int n = 0; n < 2; ++n) dst##8[n] = PG8_LD8(lds + PG8_SB(b, h) + boff + n * 2048); } else { \
;         _Pragma("unroll") for (int n = 0; n < 2; ++n) _Pragma("unroll") for (int k = 0; k < 2; ++k) dst[n][k] = *(const LAS bf16x8*)(lds + PG8_SB(b, h) + boff + n * 2048 + k * 1024); } } while (0)
; #define PG8_MM(ai, bj, At, Bt) do { if (FP8) PG8_MMA8(ai, bj, At, Bt); else PG8_MMA(ai, bj, At, Bt); } while (0)
; #define PG8_WAIT_V(n) asm volatile("s_waitcnt vmcnt(" #n ")" ::: "memory")
; #define PG8_WAIT_L(n) asm volatile("s_waitcnt lgkmcnt(" #n ")" ::: "memory")
; #define PG8_BAR __builtin_amdgcn_s_barrier()
; template <bool GATHER, class Epi, class Sched, bool FP8 = false>
; DEV void gemm_phase(LAS char* lds, const Gemm g, const Sched& S, const Epi& E) {
;     ...
;             PG8_WAIT_V(8); PG8_WAIT_L(0); PG8_BAR; PG8_MM(1, 0, At, B0); PG8_MM(1, 1, At, B1); PG8_BAR; PG8_SCHED;
;             PG8_LDB(B0, 1, 0); PG8_LDB(B1, 1, 1); PG8_SCHED; PG8_LDA(At, 1, 0); PG8_STAGE_A(PG8_SA(0, 1), a2, 1, lastn);
;             PG8_WAIT_V(8); PG8_WAIT_L(0); PG8_BAR; PG8_MM(0, 0, At, B0); PG8_MM(0, 1, At, B1); PG8_BAR; PG8_SCHED;
;             PG8_LDA(At, 1, 1); PG8_STAGE_B(PG8_SB(1, 0), b3); PG8_STAGE_B(PG8_SB(1, 1), b3 + hstepB); PG8_STAGE_A(PG8_SA(1, 0), a3, 0, lastn);
;             PG8_WAIT_V(8); PG8_WAIT_L(0); PG8_BAR; PG8_MM(1, 0, At, B0); PG8_MM(1, 1, At, B1); PG8_BAR; PG8_SCHED;
;         }
.Lp9_g1_skip:
	s_mov_b32 s2, m0
	s_mov_b32 m0, s62
	s_nop 0
	global_load_lds_dwordx4 v200, s[60:61]
	s_mov_b32 m0, s2
	s_nop 0
	s_mov_b32 s2, m0
	s_mov_b32 m0, s63
	s_nop 0
	global_load_lds_dwordx4 v202, s[60:61]
	s_mov_b32 m0, s2
	s_waitcnt vmcnt(8)
	s_waitcnt lgkmcnt(0)
	s_barrier
	s_setprio 1
	s_waitcnt lgkmcnt(6)
	v_mfma_scale_f32_16x16x128_f8f6f4 v[192:195], v[2:9], v[34:41], v[192:195], v1, v209 op_sel_hi:[0,0,0]
	v_mfma_scale_f32_16x16x128_f8f6f4 v[184:187], v[10:17], v[34:41], v[184:187], v1, v209 op_sel_hi:[0,0,0]
	s_waitcnt lgkmcnt(4)
	v_mfma_scale_f32_16x16x128_f8f6f4 v[174:177], v[2:9], v[42:49], v[174:177], v1, v209 op_sel_hi:[0,0,0]
	v_mfma_scale_f32_16x16x128_f8f6f4 v[166:169], v[10:17], v[42:49], v[166:169], v1, v209 op_sel_hi:[0,0,0]
	s_waitcnt lgkmcnt(2)
	v_mfma_scale_f32_16x16x128_f8f6f4 v[158:161], v[2:9], v[50:57], v[158:161], v1, v209 op_sel_hi:[0,0,0]
	v_mfma_scale_f32_16x16x128_f8f6f4 v[150:153], v[10:17], v[50:57], v[150:153], v1, v209 op_sel_hi:[0,0,0]
	s_waitcnt lgkmcnt(0)
	v_mfma_scale_f32_16x16x128_f8f6f4 v[142:145], v[2:9], v[58:65], v[142:145], v1, v209 op_sel_hi:[0,0,0]
	v_mfma_scale_f32_16x16x128_f8f6f4 v[134:137], v[10:17], v[58:65], v[134:137], v1, v209 op_sel_hi:[0,0,0]
	s_setprio 0
	s_setprio 1
	v_mfma_scale_f32_16x16x128_f8f6f4 v[188:191], v[18:25], v[34:41], v[188:191], v1, v209 op_sel_hi:[0,0,0]
	v_mfma_scale_f32_16x16x128_f8f6f4 v[180:183], v[26:33], v[34:41], v[180:183], v1, v209 op_sel_hi:[0,0,0]
	v_mfma_scale_f32_16x16x128_f8f6f4 v[170:173], v[18:25], v[42:49], v[170:173], v1, v209 op_sel_hi:[0,0,0]
	v_mfma_scale_f32_16x16x128_f8f6f4 v[162:165], v[26:33], v[42:49], v[162:165], v1, v209 op_sel_hi:[0,0,0]
	v_mfma_scale_f32_16x16x128_f8f6f4 v[154:157], v[18:25], v[50:57], v[154:157], v1, v209 op_sel_hi:[0,0,0]
	v_mfma_scale_f32_16x16x128_f8f6f4 v[146:149], v[26:33], v[50:57], v[146:149], v1, v209 op_sel_hi:[0,0,0]
	v_mfma_scale_f32_16x16x128_f8f6f4 v[138:141], v[18:25], v[58:65], v[138:141], v1, v209 op_sel_hi:[0,0,0]
	v_mfma_scale_f32_16x16x128_f8f6f4 v[130:133], v[26:33], v[58:65], v[130:133], v1, v209 op_sel_hi:[0,0,0]
	s_setprio 0
	s_barrier
	s_add_u32 s38, s20, 0x20080
	ds_read_b128 v[34:37], v219 offset:49152
	ds_read_b128 v[38:41], v219 offset:50176
	ds_read_b128 v[42:45], v219 offset:51200
	ds_read_b128 v[46:49], v219 offset:52224
	ds_read_b128 v[50:53], v219 offset:53248
	ds_read_b128 v[54:57], v219 offset:54272
	ds_read_b128 v[58:61], v219 offset:55296
	ds_read_b128 v[62:65], v219 offset:56320
	s_mov_b32 s2, m0
	s_mov_b32 m0, s66
	s_nop 0
	global_load_lds_dwordx4 v204, s[58:59]
	s_mov_b32 m0, s2
	s_addc_u32 s39, s21, 0
	s_mov_b32 s2, m0
	s_mov_b32 m0, s67
	s_nop 0
	global_load_lds_dwordx4 v204, s[38:39]
	s_mov_b32 m0, s2
	s_add_u32 s38, s20, 0x8080
	s_addc_u32 s39, s21, 0
	s_mov_b32 s2, m0
	s_mov_b32 m0, s70
	s_nop 0
	global_load_lds_dwordx4 v204, s[38:39]
	s_mov_b32 m0, s2
	s_add_u32 s20, s20, 0x28080
	s_addc_u32 s21, s21, 0
	s_mov_b32 s2, m0
	s_mov_b32 m0, s71
	s_nop 0
	global_load_lds_dwordx4 v204, s[20:21]
	s_mov_b32 m0, s2
	s_nop 0
	s_mov_b32 s2, m0
	s_mov_b32 m0, s68
	s_nop 0
	global_load_lds_dwordx4 v196, s[42:43]
	s_mov_b32 m0, s2
	s_nop 0
	s_mov_b32 s2, m0
	s_mov_b32 m0, s69
	s_nop 0
	global_load_lds_dwordx4 v198, s[42:43]
	s_mov_b32 m0, s2
	s_waitcnt vmcnt(8)
	s_waitcnt lgkmcnt(0)
	s_barrier
	s_setprio 1
	s_waitcnt lgkmcnt(6)
	v_mfma_scale_f32_16x16x128_f8f6f4 v[126:129], v[2:9], v[34:41], v[126:129], v1, v209 op_sel_hi:[0,0,0]
	v_mfma_scale_f32_16x16x128_f8f6f4 v[118:121], v[10:17], v[34:41], v[118:121], v1, v209 op_sel_hi:[0,0,0]
	s_waitcnt lgkmcnt(4)
	v_mfma_scale_f32_16x16x128_f8f6f4 v[110:113], v[2:9], v[42:49], v[110:113], v1, v209 op_sel_hi:[0,0,0]
	v_mfma_scale_f32_16x16x128_f8f6f4 v[102:105], v[10:17], v[42:49], v[102:105], v1, v209 op_sel_hi:[0,0,0]
	s_waitcnt lgkmcnt(2)
	v_mfma_scale_f32_16x16x128_f8f6f4 v[94:97], v[2:9], v[50:57], v[94:97], v1, v209 op_sel_hi:[0,0,0]
	v_mfma_scale_f32_16x16x128_f8f6f4 v[86:89], v[10:17], v[50:57], v[86:89], v1, v209 op_sel_hi:[0,0,0]
	s_waitcnt lgkmcnt(0)
	v_mfma_scale_f32_16x16x128_f8f6f4 v[78:81], v[2:9], v[58:65], v[78:81], v1, v209 op_sel_hi:[0,0,0]
	v_mfma_scale_f32_16x16x128_f8f6f4 v[70:73], v[10:17], v[58:65], v[70:73], v1, v209 op_sel_hi:[0,0,0]
	s_setprio 0
	s_setprio 1
	v_mfma_scale_f32_16x16x128_f8f6f4 v[122:125], v[18:25], v[34:41], v[122:125], v1, v209 op_sel_hi:[0,0,0]
	v_mfma_scale_f32_16x16x128_f8f6f4 v[114:117], v[26:33], v[34:41], v[114:117], v1, v209 op_sel_hi:[0,0,0]
	v_mfma_scale_f32_16x16x128_f8f6f4 v[106:109], v[18:25], v[42:49], v[106:109], v1, v209 op_sel_hi:[0,0,0]
	v_mfma_scale_f32_16x16x128_f8f6f4 v[98:101], v[26:33], v[42:49], v[98:101], v1, v209 op_sel_hi:[0,0,0]
	v_mfma_scale_f32_16x16x128_f8f6f4 v[90:93], v[18:25], v[50:57], v[90:93], v1, v209 op_sel_hi:[0,0,0]
	v_mfma_scale_f32_16x16x128_f8f6f4 v[82:85], v[26:33], v[50:57], v[82:85], v1, v209 op_sel_hi:[0,0,0]
	v_mfma_scale_f32_16x16x128_f8f6f4 v[74:77], v[18:25], v[58:65], v[74:77], v1, v209 op_sel_hi:[0,0,0]
	v_mfma_scale_f32_16x16x128_f8f6f4 v[66:69], v[26:33], v[58:65], v[66:69], v1, v209 op_sel_hi:[0,0,0]
	s_setprio 0
	s_barrier
	s_add_u32 s56, s56, 0x100
	s_addc_u32 s57, s57, 0
	s_cmp_ge_i32 s19, s13
	s_cbranch_scc1 .LBB0_1331
; #define PG8_STAGE_A(bufoff, gbase, hh, nx) do { if (FP8 && !GATHER) { glds16s((gbase) + (size_t)(hh) * dA2, vA[0][0], ldsb + (unsigned)(bufoff)); glds16s((gbase) + (size_t)(hh) * dA2 + dA1, vA[0][0], ldsb + (unsigned)(bufoff) + 8192u); } \
;         else PG8_STAGE2(bufoff, gbase, vA[hh][0], vA[hh][1]); } while (0)
; #define PG8_LDA(dst, b, h) do { if (FP8) { _Pragma("unroll") for (int m = 0; m < 4; ++m) dst##8[m] = PG8_LD8(lds + PG8_SA(b, h) + aoff + m * 2048); } else { \
;         _Pragma("unroll") for (int m = 0; m < 4; ++m) _Pragma("unroll") for (int k = 0; k < 2; ++k) dst[m][k] = *(const LAS bf16x8*)(lds + PG8_SA(b, h) + aoff + m * 2048 + k * 1024); } } while (0)
; #define PG8_LDB(dst, b, h) do { if (FP8) { _Pragma("unroll") for (int n = 0; n < 2; ++n) dst##8[n] = PG8_LD8(lds + PG8_SB(b, h) + boff + n * 2048); } else { \
;         _Pragma("unroll") for (int n = 0; n < 2; ++n) _Pragma("unroll") for (int k = 0; k < 2; ++k) dst[n][k] = *(const LAS bf16x8*)(lds + PG8_SB(b, h) + boff + n * 2048 + k * 1024); } } while (0)
; #define PG8_SCHED __builtin_amdgcn_sched_barrier(0)
; template <bool GATHER, class Epi, class Sched, bool FP8 = false>
; DEV void gemm_phase(LAS char* lds, const Gemm g, const Sched& S, const Epi& E) {
;     ...
;             const bool last = (t == nt - 2), lastn = last && has_next;
;             const char* a1 = cA + (size_t)(t + 1) * kstep;
;             const char* a2 = last ? nA : cA + (size_t)(t + 2) * kstep; const char* b2 = last ? nB : cB + (size_t)(t + 2) * kstep;
;             const char* a3 = a2 + kstep; const char* b3 = b2 + kstep;
;             if (GATHER && lastn) PG8_GOFF(nxt, vA, 0);
;             PG8_LDB(B0, 0, 0); PG8_LDB(B1, 0, 1); PG8_SCHED; PG8_LDA(At, 0, 0); PG8_STAGE_A(PG8_SA(1, 1), a1, 1, false);
;             if (GATHER && lastn) PG8_GOFF(nxt, vA, 1);
.LBB0_1326:
	s_cmp_eq_u32 s73, s19
	s_cselect_b64 s[58:59], -1, 0
	s_and_b64 s[20:21], s[54:55], s[58:59]
	s_cselect_b32 s100, 1, 0
	v_cndmask_b32_e64 v2, 0, 1, s[20:21]
	v_cmp_ne_u32_e64 s[42:43], 1, v2
	s_andn2_b64 vcc, exec, s[20:21]
	s_cbranch_vccnz .LBB0_1328
	v_mov_b32_e32 v2, v246
	s_nop 0
	v_ashrrev_i32_e32 v4, 31, v2
	v_lshrrev_b32_e32 v4, 26, v4
	v_lshlrev_b32_e32 v3, 4, v2
	v_add_u32_e32 v4, v2, v4
	v_bfe_i32 v2, v2, 27, 1
	v_lshrrev_b32_e32 v2, 22, v2
	v_add_u32_e32 v2, v3, v2
	v_and_b32_e32 v2, 0xfffffc00, v2
	v_sub_u32_e32 v2, v3, v2
	v_lshrrev_b32_e32 v3, 4, v2
	v_bitop3_b32 v5, v3, v2, 32 bitop3:0x6c
	v_ashrrev_i32_e32 v2, 31, v2
	v_ashrrev_i32_e32 v4, 6, v4
	v_lshrrev_b32_e32 v2, 26, v2
	v_lshlrev_b32_e32 v3, 3, v4
	v_add_u32_e32 v2, v5, v2
	v_and_b32_e32 v3, -16, v3
	v_ashrrev_i32_e32 v6, 6, v2
	v_add_u32_e32 v7, v6, v3
	v_cmp_lt_i32_e32 vcc, v7, v221
	s_nop 1
	v_cndmask_b32_e32 v2, 0, v7, vcc
	v_add_u32_e32 v2, v2, v220
	v_ashrrev_i32_e32 v3, 31, v2
	v_lshl_add_u64 v[2:3], v[2:3], 2, s[6:7]
	global_load_dword v224, v[2:3], off
	v_add_u32_e32 v2, 64, v7
	v_cmp_lt_i32_e32 vcc, v2, v221
	s_nop 1
	v_cndmask_b32_e32 v2, 0, v2, vcc
	v_add_u32_e32 v2, v2, v220
	v_ashrrev_i32_e32 v3, 31, v2
	v_lshl_add_u64 v[2:3], v[2:3], 2, s[6:7]
	global_load_dword v225, v[2:3], off
	v_lshlrev_b32_e32 v2, 5, v4
	v_mul_i32_i24_e32 v4, 64, v6
	v_sub_u32_e32 v4, v5, v4
	v_ashrrev_i16_sdwa v4, v218, sext(v4) dst_sel:DWORD dst_unused:UNUSED_PAD src0_sel:DWORD src1_sel:BYTE_0
	v_and_b32_e32 v2, 32, v2
	v_bfe_i32 v4, v4, 0, 16
	v_add_lshl_u32 v226, v2, v4, 1
.LBB0_1328:
	v_add_u32_e32 v2, 0x10000, v205
	v_add_u32_e32 v14, 0x14000, v205
	ds_read_b128 v[18:21], v2
	ds_read_b128 v[22:25], v2 offset:1024
	ds_read_b128 v[26:29], v2 offset:2048
	ds_read_b128 v[30:33], v2 offset:3072
	ds_read_b128 v[2:5], v14
	ds_read_b128 v[6:9], v14 offset:1024
	ds_read_b128 v[10:13], v14 offset:2048
	ds_read_b128 v[14:17], v14 offset:3072
	s_add_u32 s2, s4, s56
	s_addc_u32 s3, s5, s57
	s_add_u32 s20, s2, 0xffffff80
	s_addc_u32 s21, s3, -1
	ds_read_b128 v[58:61], v219
	ds_read_b128 v[62:65], v219 offset:1024
	ds_read_b128 v[50:53], v219 offset:2048
	ds_read_b128 v[54:57], v219 offset:3072
	ds_read_b128 v[42:45], v219 offset:4096
	ds_read_b128 v[46:49], v219 offset:5120
	ds_read_b128 v[34:37], v219 offset:6144
	ds_read_b128 v[38:41], v219 offset:7168
	s_mov_b32 s2, m0
	s_mov_b32 m0, s74
	s_nop 0
	global_load_lds_dwordx4 v200, s[20:21]
	s_mov_b32 m0, s2
	s_and_b64 vcc, exec, s[42:43]
	s_mov_b32 s2, m0
	s_mov_b32 m0, s75
	s_nop 0
	global_load_lds_dwordx4 v202, s[20:21]
	s_mov_b32 m0, s2
	s_cbranch_vccnz .LBB0_1325
	v_mov_b32_e32 v178, v246
	s_nop 0
	v_ashrrev_i32_e32 v199, 31, v178
	v_lshrrev_b32_e32 v199, 26, v199
	v_lshlrev_b32_e32 v197, 4, v178
	v_add_u32_e32 v199, v178, v199
	v_bfe_i32 v178, v178, 27, 1
	v_lshrrev_b32_e32 v178, 22, v178
	v_add_u32_e32 v178, v197, v178
	v_and_b32_e32 v178, 0xfffffc00, v178
	v_sub_u32_e32 v178, v197, v178
	v_lshrrev_b32_e32 v197, 4, v178
	v_bitop3_b32 v197, v197, v178, 32 bitop3:0x6c
	v_ashrrev_i32_e32 v178, 31, v178
	v_ashrrev_i32_e32 v199, 6, v199
	v_lshrrev_b32_e32 v178, 26, v178
	v_lshlrev_b32_e32 v200, 3, v199
	v_add_u32_e32 v178, v197, v178
	v_and_b32_e32 v200, -16, v200
	v_ashrrev_i32_e32 v178, 6, v178
	v_add_u32_e32 v202, v200, v178
	v_add_u32_e32 v200, 0x80, v202
	v_cmp_lt_i32_e32 vcc, v200, v221
	v_mul_i32_i24_e32 v178, 64, v178
	v_sub_u32_e32 v178, v197, v178
	v_cndmask_b32_e32 v200, 0, v200, vcc
	v_add_u32_e32 v200, v200, v220
	v_ashrrev_i32_e32 v201, 31, v200
	v_lshl_add_u64 v[200:201], v[200:201], 2, s[6:7]
	global_load_dword v227, v[200:201], off
	v_add_u32_e32 v200, 0xc0, v202
	v_cmp_lt_i32_e32 vcc, v200, v221
	v_lshlrev_b32_e32 v199, 5, v199
	v_ashrrev_i16_sdwa v178, v218, sext(v178) dst_sel:DWORD dst_unused:UNUSED_PAD src0_sel:DWORD src1_sel:BYTE_0
	v_cndmask_b32_e32 v200, 0, v200, vcc
	v_add_u32_e32 v200, v200, v220
	v_ashrrev_i32_e32 v201, 31, v200
	v_lshl_add_u64 v[200:201], v[200:201], 2, s[6:7]
	global_load_dword v228, v[200:201], off
	v_and_b32_e32 v199, 32, v199
	v_bfe_i32 v178, v178, 0, 16
	v_add_lshl_u32 v178, v199, v178, 1
	s_branch .LBB0_1325
